# baseline (speedup 1.0000x reference)
_Z8pam_prepPKfS0_S0_S0_PDv4_jS2_S2_PfS3_:
	s_load_dwordx8 s[4:11], s[0:1], 0x0
	s_load_dwordx8 s[12:19], s[0:1], 0x20
	s_load_dwordx2 s[20:21], s[0:1], 0x40
	v_and_b32_e32 v1, 63, v0
	v_lshrrev_b32_e32 v4, 6, v0
	v_and_b32_e32 v2, 31, v1
	v_lshrrev_b32_e32 v3, 5, v1
	v_readfirstlane_b32 s22, v4
	v_lshlrev_b32_e32 v14, 4, v1
	s_mul_i32 s23, s2, 0x1900
	s_lshl_b32 s30, s2, 12
	s_lshl_b32 s31, s2, 10
	s_waitcnt lgkmcnt(0)
	s_add_u32 s24, s4, s23
	s_addc_u32 s25, s5, 0
	s_add_u32 s28, s16, s30
	s_addc_u32 s29, s17, 0
	s_cmp_ge_u32 s22, 2
	s_cbranch_scc1 .Lpp_tail
	v_mul_u32_u24_e32 v5, 0xc8, v2
	v_lshl_add_u32 v5, v3, 5, v5
	v_mov_b32_e32 v40, 0
	v_mov_b32_e32 v41, 0
	v_mov_b32_e32 v42, 0
	v_mov_b32_e32 v43, 0
	v_mov_b32_e32 v44, 0
	v_mov_b32_e32 v45, 0
	v_mov_b32_e32 v46, 0
	v_mov_b32_e32 v47, 0
	global_load_dwordx4 v[16:19], v5, s[24:25] offset:0
	global_load_dwordx4 v[20:23], v5, s[24:25] offset:16
	global_load_dwordx4 v[24:27], v5, s[24:25] offset:64
	global_load_dwordx4 v[28:31], v5, s[24:25] offset:80
	global_load_dwordx4 v[32:35], v5, s[24:25] offset:128
	global_load_dwordx4 v[36:39], v5, s[24:25] offset:144
	s_mov_b32 exec_hi, 0
	global_load_dwordx2 v[40:41], v5, s[24:25] offset:192
	s_mov_b64 exec, -1
	v_mov_b32_e32 v48, 0
	v_mov_b32_e32 v49, 0
	v_mov_b32_e32 v50, 0
	v_mov_b32_e32 v51, 0
	v_mov_b32_e32 v52, 0
	v_mov_b32_e32 v53, 0
	v_mov_b32_e32 v54, 0
	v_mov_b32_e32 v55, 0
	v_mov_b32_e32 v56, 0
	v_mov_b32_e32 v57, 0
	v_mov_b32_e32 v58, 0
	v_mov_b32_e32 v59, 0
	v_mov_b32_e32 v60, 0
	v_mov_b32_e32 v61, 0
	v_mov_b32_e32 v62, 0
	v_mov_b32_e32 v63, 0
	v_mov_b32_e32 v64, 0
	v_mov_b32_e32 v65, 0
	v_mov_b32_e32 v66, 0
	v_mov_b32_e32 v67, 0
	v_mov_b32_e32 v68, 0
	v_mov_b32_e32 v69, 0
	v_mov_b32_e32 v70, 0
	v_mov_b32_e32 v71, 0
	v_mov_b32_e32 v72, 0
	v_mov_b32_e32 v73, 0
	v_mov_b32_e32 v74, 0
	v_mov_b32_e32 v75, 0
	v_mov_b32_e32 v76, 0
	v_mov_b32_e32 v77, 0
	v_mov_b32_e32 v78, 0
	v_mov_b32_e32 v79, 0
	v_mul_u32_u24_e32 v6, 0x640, v3
	v_lshl_add_u32 v6, v2, 2, v6
	s_cmp_eq_u32 s22, 1
	s_cbranch_scc1 .Lpp_w1
	v_add_u32_e32 v7, 0xc80, v6
	v_add_u32_e32 v8, 0x1900, v6
	v_add_u32_e32 v9, 0x2580, v6
	global_load_dword v48, v6, s[10:11] offset:0
	global_load_dword v49, v6, s[10:11] offset:200
	global_load_dword v50, v6, s[10:11] offset:400
	global_load_dword v51, v6, s[10:11] offset:600
	global_load_dword v52, v6, s[10:11] offset:800
	global_load_dword v53, v6, s[10:11] offset:1000
	global_load_dword v54, v6, s[10:11] offset:1200
	global_load_dword v55, v6, s[10:11] offset:1400
	global_load_dword v56, v7, s[10:11] offset:0
	global_load_dword v57, v7, s[10:11] offset:200
	global_load_dword v58, v7, s[10:11] offset:400
	global_load_dword v59, v7, s[10:11] offset:600
	global_load_dword v60, v7, s[10:11] offset:800
	global_load_dword v61, v7, s[10:11] offset:1000
	global_load_dword v62, v7, s[10:11] offset:1200
	global_load_dword v63, v7, s[10:11] offset:1400
	global_load_dword v64, v8, s[10:11] offset:0
	global_load_dword v65, v8, s[10:11] offset:200
	global_load_dword v66, v8, s[10:11] offset:400
	global_load_dword v67, v8, s[10:11] offset:600
	global_load_dword v68, v8, s[10:11] offset:800
	global_load_dword v69, v8, s[10:11] offset:1000
	global_load_dword v70, v8, s[10:11] offset:1200
	global_load_dword v71, v8, s[10:11] offset:1400
	s_mov_b64 s[44:45], exec
	s_mov_b32 exec_hi, 0
	global_load_dword v72, v9, s[10:11] offset:0
	global_load_dword v73, v9, s[10:11] offset:200
	s_mov_b64 exec, s[44:45]
	s_waitcnt vmcnt(26)
	v_cvt_pk_f16_f32 v80, v16, v17
	v_cvt_pk_f16_f32 v81, v18, v19
	v_cvt_pk_f16_f32 v82, v20, v21
	v_cvt_pk_f16_f32 v83, v22, v23
	v_cvt_pk_f16_f32 v84, v24, v25
	v_cvt_pk_f16_f32 v85, v26, v27
	v_cvt_pk_f16_f32 v86, v28, v29
	v_cvt_pk_f16_f32 v87, v30, v31
	v_cvt_pk_f16_f32 v88, v32, v33
	v_cvt_pk_f16_f32 v89, v34, v35
	v_cvt_pk_f16_f32 v90, v36, v37
	v_cvt_pk_f16_f32 v91, v38, v39
	v_cvt_pk_f16_f32 v92, v40, v41
	v_cvt_pk_f16_f32 v93, v42, v43
	v_cvt_pk_f16_f32 v94, v44, v45
	v_cvt_pk_f16_f32 v95, v46, v47
	s_waitcnt vmcnt(0)
	v_cvt_pk_f16_f32 v112, v48, v49
	v_cvt_pk_f16_f32 v113, v50, v51
	v_cvt_pk_f16_f32 v114, v52, v53
	v_cvt_pk_f16_f32 v115, v54, v55
	v_cvt_pk_f16_f32 v116, v56, v57
	v_cvt_pk_f16_f32 v117, v58, v59
	v_cvt_pk_f16_f32 v118, v60, v61
	v_cvt_pk_f16_f32 v119, v62, v63
	v_cvt_pk_f16_f32 v120, v64, v65
	v_cvt_pk_f16_f32 v121, v66, v67
	v_cvt_pk_f16_f32 v122, v68, v69
	v_cvt_pk_f16_f32 v123, v70, v71
	v_cvt_pk_f16_f32 v124, v72, v73
	v_cvt_pk_f16_f32 v125, v74, v75
	v_cvt_pk_f16_f32 v126, v76, v77
	v_cvt_pk_f16_f32 v127, v78, v79
	s_nop 1
	v_mfma_f32_32x32x16_f16 v[144:159], v[80:83], v[112:115], 0
	v_mfma_f32_32x32x16_f16 v[144:159], v[84:87], v[116:119], v[144:159]
	v_mfma_f32_32x32x16_f16 v[144:159], v[88:91], v[120:123], v[144:159]
	v_mfma_f32_32x32x16_f16 v[144:159], v[92:95], v[124:127], v[144:159]
	s_mov_b32 s32, 0
	s_branch .Lpp_vstore
